# early done signal: GEMM workgroups count themselves on the tail counter at the start of their last unit (p2 L0, p8, p9) so converters stop before the phase ends
# speedup vs baseline: 1.0260x; 1.0056x over previous
_Z4mega6Params:
	v_writelane_b32 v255, 0, 63
	s_mov_b32 s82, s2
	s_mov_b64 s[88:89], s[0:1]
	s_load_dwordx2 s[78:79], s[0:1], 0x98
	s_nop 0
	s_load_dwordx4 s[0:3], s[88:89], 0xa0
	s_mov_b32 s56, 0
	v_cmp_eq_u32_e64 s[4:5], 0, v0
	s_waitcnt lgkmcnt(0)
	v_writelane_b32 v253, s0, 0
	s_nop 1
	v_writelane_b32 v253, s1, 1
	v_writelane_b32 v253, s2, 2
	v_writelane_b32 v253, s3, 3
	s_load_dword s2, s[88:89], 0xb0
	s_mov_b64 s[0:1], exec
	v_writelane_b32 v253, s4, 4
	s_nop 1
	v_writelane_b32 v253, s5, 5
	s_and_b64 s[4:5], s[0:1], s[4:5]
	s_mov_b64 exec, s[4:5]
	s_cbranch_execz .LBB0_2
	s_mov_b32 s4, 0
	s_mov_b32 s5, s4
	s_add_i32 s3, 0, 0x25800
	s_mov_b32 s6, s4
	s_mov_b32 s7, s4
	v_mov_b64_e32 v[2:3], s[4:5]
	v_mov_b32_e32 v1, s3
	v_mov_b64_e32 v[4:5], s[6:7]
	s_add_i32 s3, 0, 0x25b00
	ds_write_b128 v1, v[2:5]
	v_mov_b32_e32 v1, s3
	s_add_i32 s3, 0, 0x25b10
	ds_write_b128 v1, v[2:5]
	v_mov_b32_e32 v1, s3
	ds_write_b128 v1, v[2:5]

.LBB0_309:
	s_add_i32 s24, s24, 1
	s_mul_i32 s38, s24, 0xf0
	s_add_i32 s38, s38, s82
	s_cmpk_lt_i32 s38, 0x3c0
	s_cselect_b64 s[8:9], -1, 0
	s_cmpk_gt_i32 s38, 0x3bf
	s_cselect_b64 s[36:37], -1, 0
	s_and_b64 vcc, exec, s[36:37]
	s_cbranch_vccz .Les_p2_skip
	v_readfirstlane_b32 s100, v0
	s_cmp_lg_u32 s100, 0
	s_cbranch_scc1 .Les_p2_flag
	v_readlane_b32 s100, v255, 18
	s_lshl_b32 s100, s100, 10
	s_add_u32 s100, s100, 0x5100
	v_readlane_b32 s101, v255, 5
	s_add_u32 s100, s100, s101
	v_readlane_b32 s101, v255, 6
	s_addc_u32 s101, s101, 0
	s_mov_b64 exec, 1
	global_atomic_add v195, v197, s[100:101]
	s_mov_b64 exec, -1
.Les_p2_flag:
	v_writelane_b32 v255, 1, 63
.Les_p2_skip:
	s_cbranch_vccnz .LBB0_311
	s_ashr_i32 s6, s38, 31
	s_lshr_b32 s6, s6, 29
	s_add_i32 s6, s38, s6
	s_ashr_i32 s7, s6, 3
	s_and_b32 s6, s6, -8
	s_sub_i32 s6, s38, s6
	s_cmp_lt_i32 s6, 0
	s_movk_i32 s25, 0x79
	s_cselect_b32 s25, s25, 0x78
	s_mul_i32 s6, s25, s6
	s_add_i32 s6, s6, s7
	s_mul_hi_i32 s7, s6, 0x88888889
	s_add_i32 s7, s7, s6
	s_lshr_b32 s25, s7, 31
	s_ashr_i32 s7, s7, 7
	s_add_i32 s7, s7, s25
	s_lshl_b32 s25, s7, 3
	s_mulk_i32 s7, 0xf0
	s_sub_i32 s6, s6, s7
	s_bfe_u32 s7, s6, 0x3001c
	s_add_i32 s7, s6, s7
	s_sext_i32_i16 s26, s7
	s_and_b32 s7, s7, 0xfff8
	s_sub_i32 s6, s6, s7
	s_sext_i32_i16 s6, s6
	s_lshr_b32 s38, s26, 3
	s_add_i32 s40, s25, s6
	s_ashr_i32 s41, s40, 31
	s_bfe_i64 s[26:27], s[38:39], 0x100000
	s_lshl_b64 s[6:7], s[40:41], 20
	s_lshl_b64 s[26:27], s[26:27], 20
	s_lshl_b32 s33, s40, 8
	s_lshl_b32 s25, s38, 8

.LBB0_317:
	v_readlane_b32 s100, v255, 63
	v_writelane_b32 v255, 0, 63
	s_add_u32 s4, s0, 0x5100
	s_addc_u32 s5, s1, 0
	s_waitcnt vmcnt(0) lgkmcnt(0)
	s_barrier
	s_mov_b64 s[6:7], exec
	v_readlane_b32 s8, v253, 4
	v_readlane_b32 s9, v253, 5
	s_and_b64 s[8:9], s[6:7], s[8:9]
	s_mov_b64 exec, s[8:9]
	s_cbranch_execz .LBB0_320
	s_cmp_lg_u32 s100, 0
	s_cbranch_scc1 .LBB0_320
	s_mov_b64 s[8:9], exec
	v_mbcnt_lo_u32_b32 v1, s8, 0
	v_mbcnt_hi_u32_b32 v1, s9, v1
	v_cmp_eq_u32_e32 vcc, 0, v1
	s_and_b64 s[16:17], exec, vcc
	s_mov_b64 exec, s[16:17]
	s_cbranch_execz .LBB0_320
	s_bcnt1_i32_b64 s2, s[8:9]
	v_mov_b32_e32 v1, s2
	global_atomic_add v195, v1, s[4:5]

.LBB0_1000:
	s_mov_b64 s[6:7], 0
	s_andn2_b64 vcc, exec, s[8:9]
	s_cbranch_vccz .Les_p8_skip
	v_readfirstlane_b32 s100, v0
	s_cmp_lg_u32 s100, 0
	s_cbranch_scc1 .Les_p8_flag
	v_readlane_b32 s100, v255, 18
	s_lshl_b32 s100, s100, 10
	s_add_u32 s100, s100, 0x5300
	v_readlane_b32 s101, v255, 5
	s_add_u32 s100, s100, s101
	v_readlane_b32 s101, v255, 6
	s_addc_u32 s101, s101, 0
	s_mov_b64 exec, 1
	global_atomic_add v195, v197, s[100:101]
	s_mov_b64 exec, -1

.Les_p8_skip:
	v_mov_b32_e32 v4, s44
	v_mov_b64_e32 v[2:3], s[42:43]
	v_mov_b32_e32 v5, s73
	s_cbranch_vccnz .LBB0_1002
	v_readlane_b32 s6, v254, 61
	s_nop 1
	v_mov_b32_e32 v2, s6
	ds_read2_b32 v[2:3], v2 offset1:1
	v_readlane_b32 s6, v254, 62
	s_waitcnt lgkmcnt(0)
	v_mul_lo_u32 v2, v2, 11
	v_mov_b32_e32 v4, s6
	v_readlane_b32 s6, v254, 63
	v_cmp_ge_i32_e32 vcc, s14, v2
	v_mul_lo_u32 v3, v3, 11
	v_mov_b32_e32 v6, s6
	v_readlane_b32 s6, v255, 0
	v_cndmask_b32_e64 v2, 0, 1, vcc
	v_cmp_ge_i32_e32 vcc, s14, v3
	v_mov_b32_e32 v8, s6
	ds_read2_b32 v[4:5], v4 offset1:1
	ds_read2_b32 v[6:7], v6 offset1:1
	ds_read2_b32 v[8:9], v8 offset1:1
	v_cndmask_b32_e64 v3, 0, 1, vcc
	v_readlane_b32 s6, v255, 1
	s_waitcnt lgkmcnt(0)
	v_mul_lo_u32 v4, v4, 11
	v_cmp_ge_i32_e32 vcc, s14, v4
	v_mul_lo_u32 v4, v6, 11
	s_nop 0
	v_addc_co_u32_e32 v2, vcc, v3, v2, vcc
	v_mul_lo_u32 v3, v5, 11
	v_cmp_ge_i32_e32 vcc, s14, v3
	s_nop 1
	v_cndmask_b32_e64 v3, 0, 1, vcc
	v_cmp_ge_i32_e32 vcc, s14, v4
	v_mul_lo_u32 v4, v8, 11
	s_nop 0
	v_addc_co_u32_e32 v2, vcc, v2, v3, vcc
	v_mul_lo_u32 v3, v7, 11
	v_cmp_ge_i32_e32 vcc, s14, v3
	s_nop 1
	v_cndmask_b32_e64 v3, 0, 1, vcc
	v_cmp_ge_i32_e32 vcc, s14, v4
	s_nop 1
	v_addc_co_u32_e32 v8, vcc, v2, v3, vcc
	v_mul_lo_u32 v2, v9, 11
	v_cmp_ge_i32_e32 vcc, s14, v2
	v_mov_b32_e32 v2, s6
	ds_read2_b32 v[2:3], v2 offset1:1
	v_readlane_b32 s6, v255, 2
	v_cndmask_b32_e64 v9, 0, 1, vcc
	s_waitcnt lgkmcnt(0)
	v_mul_lo_u32 v2, v2, 11
	v_mov_b32_e32 v4, s6
	v_readlane_b32 s6, v255, 3
	v_cmp_ge_i32_e32 vcc, s14, v2
	v_mul_lo_u32 v3, v3, 11
	v_mov_b32_e32 v6, s6
	v_readlane_b32 s6, v255, 4
	v_addc_co_u32_e32 v2, vcc, v8, v9, vcc
	s_nop 0
	v_mov_b32_e32 v10, s6
	ds_read2_b32 v[4:5], v4 offset1:1
	ds_read2_b32 v[6:7], v6 offset1:1
	ds_read_b32 v10, v10
	v_cmp_ge_i32_e32 vcc, s14, v3
	s_mov_b32 s6, 0x580000
	s_waitcnt lgkmcnt(0)
	v_mul_lo_u32 v4, v4, 11
	v_cndmask_b32_e64 v3, 0, 1, vcc
	v_cmp_ge_i32_e32 vcc, s14, v4
	v_mul_lo_u32 v4, v6, 11
	s_nop 0
	v_addc_co_u32_e32 v2, vcc, v2, v3, vcc
	v_mul_lo_u32 v3, v5, 11
	v_cmp_ge_i32_e32 vcc, s14, v3
	s_nop 1
	v_cndmask_b32_e64 v3, 0, 1, vcc
	v_cmp_ge_i32_e32 vcc, s14, v4
	v_mul_lo_u32 v4, v10, 11
	s_nop 0
	v_addc_co_u32_e32 v2, vcc, v2, v3, vcc
	v_mul_lo_u32 v3, v7, 11
	v_cmp_ge_i32_e32 vcc, s14, v3
	s_nop 1
	v_cndmask_b32_e64 v3, 0, 1, vcc
	v_cmp_ge_i32_e32 vcc, s14, v4
	s_nop 1
	v_addc_co_u32_e32 v4, vcc, v2, v3, vcc
	v_lshlrev_b32_e32 v2, 2, v4
	v_add_u32_e32 v2, 0, v2
	v_add_u32_e32 v2, 0x25840, v2
	ds_read2_b32 v[2:3], v2 offset1:1
	s_waitcnt lgkmcnt(0)
	v_sub_u32_e32 v3, v3, v2
	v_sub_u32_e32 v5, 0, v3
	v_max_i32_e32 v5, v3, v5
	v_cvt_f32_u32_e32 v6, v5
	v_mul_lo_u32 v7, v2, -11
	v_sub_u32_e32 v10, 0, v5
	v_add_u32_e32 v7, s14, v7
	v_rcp_iflag_f32_e32 v6, v6
	v_sub_u32_e32 v9, 0, v7
	v_max_i32_e32 v9, v7, v9
	v_xor_b32_e32 v8, v7, v3
	v_mul_f32_e32 v6, 0x4f7ffffe, v6
	v_cvt_u32_f32_e32 v6, v6
	v_ashrrev_i32_e32 v8, 31, v8
	v_add_u32_e32 v2, v7, v2
	v_mul_lo_u32 v10, v10, v6
	v_mul_hi_u32 v10, v6, v10
	v_add_u32_e32 v6, v6, v10
	v_mul_hi_u32 v6, v9, v6
	v_mul_lo_u32 v10, v6, v5
	v_sub_u32_e32 v9, v9, v10
	v_add_u32_e32 v10, 1, v6
	v_sub_u32_e32 v11, v9, v5
	v_cmp_ge_u32_e32 vcc, v9, v5
	s_nop 1
	v_cndmask_b32_e32 v6, v6, v10, vcc
	v_cndmask_b32_e32 v9, v9, v11, vcc
	v_add_u32_e32 v10, 1, v6
	v_cmp_ge_u32_e32 vcc, v9, v5
	s_nop 1
	v_cndmask_b32_e32 v5, v6, v10, vcc
	v_xor_b32_e32 v5, v5, v8
	v_sub_u32_e32 v6, v5, v8
	v_mul_lo_u32 v3, v6, v3
	v_ashrrev_i32_e32 v7, 31, v6
	v_sub_u32_e32 v8, v2, v3
	v_mul_hi_u32 v3, v4, s6
	v_mul_lo_u32 v2, v4, s6
	v_lshlrev_b64 v[4:5], 19, v[6:7]
	v_lshl_add_u64 v[2:3], v[2:3], 0, v[4:5]
	v_lshlrev_b32_e32 v4, 8, v8
	v_lshlrev_b32_e32 v5, 8, v6
	s_mov_b64 s[6:7], -1

.LBB0_1013:
	v_readlane_b32 s100, v255, 63
	v_writelane_b32 v255, 0, 63
	v_readlane_b32 s4, v255, 18
	s_lshl_b32 s6, s4, 8
	s_ashr_i32 s7, s6, 31
	v_readlane_b32 s5, v255, 19
	s_add_u32 s4, s0, 0x5000
	s_addc_u32 s5, s1, 0
	s_lshl_b64 s[6:7], s[6:7], 2
	s_add_u32 s6, s4, s6
	s_addc_u32 s7, s5, s7
	s_waitcnt vmcnt(0) lgkmcnt(0)
	s_barrier
	s_mov_b64 s[8:9], exec
	v_readlane_b32 s16, v253, 4
	v_readlane_b32 s17, v253, 5
	s_and_b64 s[16:17], s[8:9], s[16:17]
	s_mov_b64 exec, s[16:17]
	s_cbranch_execz .LBB0_1016
	s_cmp_lg_u32 s100, 0
	s_cbranch_scc1 .LBB0_1016
	s_mov_b64 s[22:23], exec
	v_mbcnt_lo_u32_b32 v1, s22, 0
	v_mbcnt_hi_u32_b32 v1, s23, v1
	v_cmp_eq_u32_e32 vcc, 0, v1
	s_and_b64 s[16:17], exec, vcc
	s_mov_b64 exec, s[16:17]
	s_cbranch_execz .LBB0_1016
	s_bcnt1_i32_b64 s2, s[22:23]
	v_mov_b32_e32 v1, s2
	global_atomic_add v195, v1, s[6:7] offset:768

.LBB0_1190:
	s_mov_b64 s[8:9], 0
	s_andn2_b64 vcc, exec, s[38:39]
	s_cbranch_vccz .Les_p9_skip
	v_readfirstlane_b32 s100, v0
	s_cmp_lg_u32 s100, 0
	s_cbranch_scc1 .Les_p9_flag
	v_readlane_b32 s100, v255, 18
	s_lshl_b32 s100, s100, 10
	s_add_u32 s100, s100, 0x5400
	v_readlane_b32 s101, v255, 5
	s_add_u32 s100, s100, s101
	v_readlane_b32 s101, v255, 6
	s_addc_u32 s101, s101, 0
	s_mov_b64 exec, 1
	global_atomic_add v195, v197, s[100:101]
	s_mov_b64 exec, -1

.Les_p9_skip:
	v_mov_b32_e32 v185, s53
	v_mov_b64_e32 v[2:3], s[26:27]
	v_mov_b64_e32 v[4:5], s[36:37]
	v_mov_b32_e32 v186, s52
	s_cbranch_vccnz .LBB0_1192
	v_readlane_b32 s8, v254, 61
	s_mov_b32 s9, 0x60000
	s_nop 0
	v_mov_b32_e32 v2, s8
	ds_read2_b32 v[2:3], v2 offset1:1
	v_readlane_b32 s8, v254, 62
	s_waitcnt lgkmcnt(0)
	v_lshlrev_b32_e32 v2, 3, v2
	v_mov_b32_e32 v4, s8
	v_readlane_b32 s8, v254, 63
	v_cmp_ge_i32_e32 vcc, v6, v2
	v_lshlrev_b32_e32 v3, 3, v3
	v_mov_b32_e32 v7, s8
	v_readlane_b32 s8, v255, 0
	v_cndmask_b32_e64 v2, 0, 1, vcc
	v_cmp_ge_i32_e32 vcc, v6, v3
	v_mov_b32_e32 v10, s8
	ds_read2_b32 v[4:5], v4 offset1:1
	ds_read2_b32 v[8:9], v7 offset1:1
	ds_read2_b32 v[10:11], v10 offset1:1
	v_cndmask_b32_e64 v3, 0, 1, vcc
	v_readlane_b32 s8, v255, 1
	s_waitcnt lgkmcnt(0)
	v_lshlrev_b32_e32 v4, 3, v4
	v_cmp_ge_i32_e32 vcc, v6, v4
	v_lshlrev_b32_e32 v4, 3, v8
	s_nop 0
	v_addc_co_u32_e32 v2, vcc, v3, v2, vcc
	v_lshlrev_b32_e32 v3, 3, v5
	v_cmp_ge_i32_e32 vcc, v6, v3
	s_nop 1
	v_cndmask_b32_e64 v3, 0, 1, vcc
	v_cmp_ge_i32_e32 vcc, v6, v4
	v_lshlrev_b32_e32 v4, 3, v10
	s_nop 0
	v_addc_co_u32_e32 v2, vcc, v2, v3, vcc
	v_lshlrev_b32_e32 v3, 3, v9
	v_cmp_ge_i32_e32 vcc, v6, v3
	s_nop 1
	v_cndmask_b32_e64 v3, 0, 1, vcc
	v_cmp_ge_i32_e32 vcc, v6, v4
	s_nop 1
	v_addc_co_u32_e32 v7, vcc, v2, v3, vcc
	v_lshlrev_b32_e32 v2, 3, v11
	v_cmp_ge_i32_e32 vcc, v6, v2
	v_mov_b32_e32 v2, s8
	ds_read2_b32 v[2:3], v2 offset1:1
	v_readlane_b32 s8, v255, 2
	v_cndmask_b32_e64 v10, 0, 1, vcc
	s_waitcnt lgkmcnt(0)
	v_lshlrev_b32_e32 v2, 3, v2
	v_mov_b32_e32 v4, s8
	v_readlane_b32 s8, v255, 3
	v_cmp_ge_i32_e32 vcc, v6, v2
	v_lshlrev_b32_e32 v3, 3, v3
	v_mov_b32_e32 v8, s8
	v_readlane_b32 s8, v255, 4
	v_addc_co_u32_e32 v2, vcc, v7, v10, vcc
	s_nop 0
	v_mov_b32_e32 v11, s8
	ds_read2_b32 v[4:5], v4 offset1:1
	ds_read2_b32 v[8:9], v8 offset1:1
	ds_read_b32 v11, v11
	v_cmp_ge_i32_e32 vcc, v6, v3
	s_mov_b32 s8, 0x300000
	s_waitcnt lgkmcnt(0)
	v_lshlrev_b32_e32 v4, 3, v4
	v_cndmask_b32_e64 v3, 0, 1, vcc
	v_cmp_ge_i32_e32 vcc, v6, v4
	v_lshlrev_b32_e32 v4, 3, v8
	s_nop 0
	v_addc_co_u32_e32 v2, vcc, v2, v3, vcc
	v_lshlrev_b32_e32 v3, 3, v5
	v_cmp_ge_i32_e32 vcc, v6, v3
	s_nop 1
	v_cndmask_b32_e64 v3, 0, 1, vcc
	v_cmp_ge_i32_e32 vcc, v6, v4
	v_lshlrev_b32_e32 v4, 3, v11
	s_nop 0
	v_addc_co_u32_e32 v2, vcc, v2, v3, vcc
	v_lshlrev_b32_e32 v3, 3, v9
	v_cmp_ge_i32_e32 vcc, v6, v3
	s_nop 1
	v_cndmask_b32_e64 v3, 0, 1, vcc
	v_cmp_ge_i32_e32 vcc, v6, v4
	s_nop 1
	v_addc_co_u32_e32 v4, vcc, v2, v3, vcc
	v_lshlrev_b32_e32 v2, 2, v4
	v_add_u32_e32 v2, 0, v2
	v_add_u32_e32 v2, 0x25840, v2
	ds_read2_b32 v[2:3], v2 offset1:1
	s_waitcnt lgkmcnt(0)
	v_sub_u32_e32 v3, v3, v2
	v_sub_u32_e32 v5, 0, v3
	v_max_i32_e32 v5, v3, v5
	v_cvt_f32_u32_e32 v7, v5
	v_lshlrev_b32_e32 v8, 3, v2
	v_sub_u32_e32 v10, 0, v5
	v_sub_u32_e32 v6, v6, v8
	v_rcp_iflag_f32_e32 v7, v7
	v_sub_u32_e32 v9, 0, v6
	v_max_i32_e32 v9, v6, v9
	v_xor_b32_e32 v8, v6, v3
	v_mul_f32_e32 v7, 0x4f7ffffe, v7
	v_cvt_u32_f32_e32 v7, v7
	v_ashrrev_i32_e32 v8, 31, v8
	v_mul_lo_u32 v10, v10, v7
	v_mul_hi_u32 v10, v7, v10
	v_add_u32_e32 v7, v7, v10
	v_mul_hi_u32 v7, v9, v7
	v_mul_lo_u32 v10, v7, v5
	v_sub_u32_e32 v9, v9, v10
	v_add_u32_e32 v10, 1, v7
	v_sub_u32_e32 v11, v9, v5
	v_cmp_ge_u32_e32 vcc, v9, v5
	s_nop 1
	v_cndmask_b32_e32 v7, v7, v10, vcc
	v_cndmask_b32_e32 v9, v9, v11, vcc
	v_add_u32_e32 v10, 1, v7
	v_cmp_ge_u32_e32 vcc, v9, v5
	s_nop 1
	v_cndmask_b32_e32 v5, v7, v10, vcc
	v_xor_b32_e32 v5, v5, v8
	v_sub_u32_e32 v8, v5, v8
	v_mul_lo_u32 v3, v8, v3
	v_sub_u32_e32 v3, v6, v3
	v_add_u32_e32 v9, v3, v2
	v_mul_hi_u32 v5, v4, s8
	v_mul_lo_u32 v4, v4, s8
	v_mul_hi_i32 v7, v8, s9
	v_mul_lo_u32 v6, v8, s9
	v_mul_hi_i32 v3, v9, s9
	v_mul_lo_u32 v2, v9, s9
	v_lshl_add_u64 v[4:5], v[4:5], 0, v[6:7]
	v_lshlrev_b32_e32 v185, 8, v9
	v_lshlrev_b32_e32 v186, 8, v8
	s_mov_b64 s[8:9], -1

.LBB0_1199:
	v_readlane_b32 s100, v255, 63
	v_writelane_b32 v255, 0, 63
	v_readlane_b32 s6, v255, 18
	s_lshl_b32 s2, s6, 8
	v_readlane_b32 s7, v255, 19
	s_add_i32 s6, s2, 0x100
	s_ashr_i32 s7, s6, 31
	s_add_u32 s46, s28, 0x5000
	s_addc_u32 s47, s29, 0
	s_lshl_b64 s[6:7], s[6:7], 2
	s_add_u32 s6, s46, s6
	s_addc_u32 s7, s47, s7
	s_waitcnt vmcnt(0) lgkmcnt(0)
	s_barrier
	s_mov_b64 s[8:9], exec
	v_readlane_b32 s16, v253, 4
	v_readlane_b32 s17, v253, 5
	s_and_b64 s[16:17], s[8:9], s[16:17]
	s_mov_b64 exec, s[16:17]
	s_cbranch_execz .LBB0_1202
	s_cmp_lg_u32 s100, 0
	s_cbranch_scc1 .LBB0_1202
	s_mov_b64 s[26:27], exec
	v_mbcnt_lo_u32_b32 v1, s26, 0
	v_mbcnt_hi_u32_b32 v1, s27, v1
	v_cmp_eq_u32_e32 vcc, 0, v1
	s_and_b64 s[16:17], exec, vcc
	s_mov_b64 exec, s[16:17]
	s_cbranch_execz .LBB0_1202
	s_bcnt1_i32_b64 s2, s[26:27]
	v_mov_b32_e32 v1, s2
	global_atomic_add v195, v1, s[6:7]
